# speedup vs baseline: 1.0605x; 1.0183x over previous
.LBB0_42:
	ds_read_b128 v[4:7], v34
	v_add_u32_e32 v2, 0x400, v2
	v_cmp_lt_u32_e32 vcc, s4, v2
	v_add_u32_e32 v34, 0x4000, v34
	s_or_b64 s[0:1], vcc, s[0:1]
	s_waitcnt lgkmcnt(0)
	global_store_dwordx4 v[0:1], v[4:7], off sc0 sc1
	v_lshl_add_u64 v[0:1], v[0:1], 0, s[2:3]
	s_andn2_b64 exec, exec, s[0:1]
	s_cbranch_execnz .LBB0_42

.LBB1_233:
	s_or_b64 exec, exec, s[4:5]
	v_min_i32_e32 v2, v14, v25
	v_cmp_gt_i32_e32 vcc, v2, v0
	s_waitcnt lgkmcnt(0)
	s_barrier
	s_and_saveexec_b64 s[2:3], vcc
	s_cbranch_execz .LBB1_242
	v_min_i32_e32 v4, 0x2000, v2
	v_add_u32_e32 v4, 3, v4
	v_ashrrev_i32_e32 v4, 2, v4
	v_cmp_lt_i32_e32 vcc, v0, v4
	s_and_b64 exec, exec, vcc
	s_cbranch_execz .LBB1_242
	v_lshlrev_b32_e32 v1, 4, v0
	ds_read_b128 v[6:9], v1
	ds_read_b128 v[14:17], v1 offset:16384
	s_lshr_b32 s4, s56, 2
	v_or_b32_e32 v2, s4, v0
	v_mov_b32_e32 v3, 0
	v_lshl_add_u64 v[10:11], v[2:3], 4, s[52:53]
	v_or_b32_e32 v5, 0x400, v0
	v_cmp_lt_i32_e32 vcc, v5, v4
	v_add_u32_e32 v2, 0x400, v2
	v_lshl_add_u64 v[12:13], v[2:3], 4, s[52:53]
	s_waitcnt lgkmcnt(1)
	global_store_dwordx4 v[10:11], v[6:9], off sc0 sc1
	s_and_b64 exec, exec, vcc
	s_cbranch_execz .LBB1_242
	s_waitcnt lgkmcnt(0)
	global_store_dwordx4 v[12:13], v[14:17], off sc0 sc1

.Ldec_noidx:
	ds_read2st64_b32 v[100:101], v105 offset1:1
	ds_read2st64_b32 v[98:99], v105 offset0:2 offset1:3
	v_mfma_f32_16x16x32_f16 v[88:91], v[76:79], v[108:111], v[88:91]
	v_cmp_lt_u32_e64 s[6:7], s19, v102
	s_or_b64 s[16:17], s[6:7], s[16:17]
	s_nop 5
	v_cndmask_b32_e64 v80, v80, v88, s[4:5]
	s_waitcnt lgkmcnt(0)
	v_add_f32_e32 v80, s12, v80
	v_mul_f32_e32 v80, 0xbfb8aa3b, v80
	v_exp_f32_e32 v80, v80
	s_waitcnt vmcnt(2)
	v_mov_b32_e32 v88, v118
	v_mov_b32_e32 v89, v119
	v_mov_b32_e32 v90, v120
	v_add_f32_e32 v80, 1.0, v80
	v_rcp_f32_e32 v80, v80
	v_mov_b32_e32 v91, v121
	global_store_dword v[134:135], v80, off sc0 sc1
	v_mov_b64_e32 v[80:81], v[84:85]
	v_mov_b64_e32 v[82:83], v[86:87]
	s_waitcnt vmcnt(1)
	v_mov_b32_e32 v84, v122
	v_mov_b32_e32 v85, v123
	v_mov_b32_e32 v86, v124
	v_mov_b32_e32 v87, v125
	s_andn2_b64 exec, exec, s[16:17]
	s_cbranch_execnz .LBB2_2
